# code placement: 4-byte pads so the P7 and P8 MFMA loops sit at the baseline's 8-byte phase
# baseline (speedup 1.0000x reference)
; #define LAS __attribute__((address_space(3)))
; __device__ __forceinline__ void moe_tables(Ctx& X) {
;     LAS int* tab = (LAS int*)(X.lds + LDS_TAB);
;     if (X.tid < 64) { const int e = X.tid;
;         const int cnt = (e < NE) ? (int)__hip_atomic_load(XP_ctl(X) + CW_CNT + 64 * e, __ATOMIC_RELAXED, __HIP_MEMORY_SCOPE_AGENT) : 0; const int k = (cnt + 255) >> 8;
; __global__ void __launch_bounds__(NTHR, 2) fwd(Args args) {
;     ...
;     if (IN(7)) { moe_tables(X); MoeSched S{(const LAS int*)(X.lds + LDS_TAB), (const char*)XP_U2(X), (const char*)XP_WguT(X), (size_t)16 * PAN_GU, XP_LIST(X), D / 2, (2 * DFF) / 256, X.G, X.bid}; EpiGateUp E{XP_ACT(X), XP_b_gu(X)};
.LBB0_884:
	s_nop 0
	s_cmp_gt_i32 s94, 7
	s_cselect_b64 s[4:5], -1, 0
	s_cmp_lt_i32 s94, 8
	s_cselect_b64 s[6:7], -1, 0
	s_and_b64 s[6:7], s[6:7], s[2:3]
	s_andn2_b64 vcc, exec, s[6:7]
	s_cbranch_vccnz .LBB0_937
	v_cmp_gt_u32_e32 vcc, 64, v0
	s_and_saveexec_b64 s[8:9], vcc
	s_cbranch_execz .LBB0_917
	v_cmp_gt_u32_e64 s[2:3], 32, v0
	s_waitcnt vmcnt(4)
	v_mov_b32_e32 v2, 0
	s_and_saveexec_b64 s[10:11], s[2:3]
	s_cbranch_execz .LBB0_888
	v_lshlrev_b32_e32 v2, 8, v0
	v_mov_b32_e32 v3, 0
	v_lshl_add_u64 v[2:3], s[90:91], 0, v[2:3]
	v_add_co_u32_e32 v2, vcc, 0x10000, v2
	s_nop 1
	v_addc_co_u32_e32 v3, vcc, 0, v3, vcc
	global_load_dword v2, v[2:3], off sc1

; #define LAS __attribute__((address_space(3)))
; __device__ __forceinline__ void moe_tables(Ctx& X) {
;     LAS int* tab = (LAS int*)(X.lds + LDS_TAB);
;     if (X.tid < 64) { const int e = X.tid;
;         const int cnt = (e < NE) ? (int)__hip_atomic_load(XP_ctl(X) + CW_CNT + 64 * e, __ATOMIC_RELAXED, __HIP_MEMORY_SCOPE_AGENT) : 0; const int k = (cnt + 255) >> 8;
; __global__ void __launch_bounds__(NTHR, 2) fwd(Args args) {
;     ...
;     if (IN(8)) { if (!IN(7)) moe_tables(X); MoeSchedDirect S{     (const LAS int*)(X.lds + LDS_TAB), (const char*)XP_ACT(X), (const char*)XP_WdT(X), (size_t)16 * PAN_D, DFF / 2, D / 256, X.G, X.bid}; EpiDown E{XP_YR(X), XP_b_d(X)};
.LBB0_987:
	s_nop 0
	s_cmp_lt_i32 s94, 9
	s_cselect_b64 s[6:7], -1, 0
	s_and_b64 s[6:7], s[6:7], s[2:3]
	s_waitcnt vmcnt(0)
	v_cndmask_b32_e64 v2, 0, 1, s[4:5]
	s_andn2_b64 vcc, exec, s[6:7]
	v_cmp_ne_u32_e64 s[2:3], 1, v2
	s_cbranch_vccnz .LBB0_1041
	s_and_b64 vcc, exec, s[2:3]
	s_cbranch_vccnz .LBB0_1022
	v_cmp_gt_u32_e32 vcc, 64, v0
	s_and_saveexec_b64 s[8:9], vcc
	s_cbranch_execz .LBB0_1021
	v_cmp_gt_u32_e64 s[4:5], 32, v0
	v_mov_b32_e32 v2, 0
	s_and_saveexec_b64 s[10:11], s[4:5]
	s_cbranch_execz .LBB0_992
	v_lshlrev_b32_e32 v2, 8, v0
	v_mov_b32_e32 v3, 0
	v_lshl_add_u64 v[2:3], s[90:91], 0, v[2:3]
	v_add_co_u32_e32 v2, vcc, 0x10000, v2
	s_nop 1
	v_addc_co_u32_e32 v3, vcc, 0, v3, vcc
	global_load_dword v2, v[2:3], off sc1
